# unit-scheduler LDS read merging: P11/P12 unit headers issue the unit-total read with the prefix-table lane read, and the start/prefix pair with the count read (2 LDS round trips per unit instead of 4)
# speedup vs baseline: 1.0024x; 1.0024x over previous
.LBB0_1270:
	ds_read_b32 v2, v246
	v_lshlrev_b32_e32 v3, 2, v194
	v_add_u32_e32 v3, 0x20100, v3
	ds_read_b32 v3, v3
	s_add_i32 s96, s96, 1
	v_readlane_b32 s9, v254, 33
	s_mul_i32 s9, s96, s9
	s_add_i32 s9, s21, s9
	s_waitcnt lgkmcnt(0)
	v_readfirstlane_b32 s30, v2
	s_min_i32 s30, s30, s23
	s_cmp_le_i32 s30, s9
	s_cselect_b64 s[48:49], -1, 0
	s_cmp_gt_i32 s30, s9
	s_cselect_b64 s[30:31], -1, 0
	s_and_b64 vcc, exec, s[48:49]
	s_cbranch_vccnz .LBB0_1272
	v_cmp_ge_i32_e32 vcc, s9, v3
	s_and_b32 vcc_lo, vcc_lo, -2
	s_bcnt1_i32_b32 s12, vcc_lo
	s_lshl_b32 s28, s12, 2
	s_add_i32 s28, s28, 0
	s_add_i32 s28, s28, 0x20100
	v_mov_b32_e32 v4, s28
	ds_read2st64_b32 v[2:3], v4 offset1:1
	ds_read_b32 v5, v4 offset:512
	s_waitcnt lgkmcnt(0)
	v_readfirstlane_b32 s28, v2
	s_sub_i32 s9, s9, s28
	s_abs_i32 s44, s9
	v_readfirstlane_b32 s35, v3
	v_readfirstlane_b32 s43, v5
	s_add_i32 s28, s43, 0xff
	s_ashr_i32 s28, s28, 8
	s_abs_i32 s45, s28
	v_cvt_f32_u32_e32 v2, s45
	s_sub_i32 s46, 0, s45
	s_xor_b32 s42, s9, s28
	s_ashr_i32 s42, s42, 31
	v_rcp_iflag_f32_e32 v2, v2
	s_nop 0
	v_mul_f32_e32 v2, 0x4f7ffffe, v2
	v_cvt_u32_f32_e32 v2, v2
	s_nop 0
	v_readfirstlane_b32 s47, v2
	s_mul_i32 s46, s46, s47
	s_mul_hi_u32 s46, s47, s46
	s_add_i32 s47, s47, s46
	s_mul_hi_u32 s46, s44, s47
	s_mul_i32 s47, s46, s45
	s_sub_i32 s44, s44, s47
	s_add_i32 s47, s46, 1
	s_sub_i32 s50, s44, s45
	s_cmp_ge_u32 s44, s45
	s_cselect_b32 s46, s47, s46
	s_cselect_b32 s44, s50, s44
	s_add_i32 s47, s46, 1
	s_cmp_ge_u32 s44, s45
	s_cselect_b32 s44, s47, s46
	s_xor_b32 s44, s44, s42
	s_sub_i32 s46, s44, s42
	s_mul_i32 s28, s28, s46
	s_sub_i32 s9, s9, s28
	s_lshl_b32 s9, s9, 8
	s_add_i32 s42, s9, s35
	s_lshl_b64 s[44:45], s[12:13], 23
	s_add_u32 s28, s60, s44
	s_addc_u32 s35, s61, s45
	s_ashr_i32 s47, s46, 31
	s_lshl_b64 s[44:45], s[46:47], 19
	s_add_u32 s44, s28, s44
	s_addc_u32 s45, s35, s45
	s_lshl_b32 s65, s46, 7
	s_sub_i32 s9, s43, s9
	v_readlane_b32 s46, v254, 38
	s_min_i32 s28, s9, 0x100
	v_readlane_b32 s47, v254, 39

.LBB0_1502:
	ds_read_b32 v2, v226
	v_lshlrev_b32_e32 v3, 2, v194
	v_add_u32_e32 v3, 0x20100, v3
	ds_read_b32 v3, v3
	s_add_i32 s2, s2, 1
	v_readlane_b32 s18, v254, 33
	s_mul_i32 s18, s2, s18
	s_add_i32 s21, s59, s18
	s_waitcnt lgkmcnt(0)
	v_readfirstlane_b32 s18, v2
	s_min_i32 s23, s18, s60
	s_cmp_gt_i32 s23, s21
	s_cselect_b64 s[18:19], -1, 0
	s_cmp_le_i32 s23, s21
	s_cbranch_scc1 .LBB0_1504
	v_cmp_ge_i32_e32 vcc, s21, v3
	s_and_b32 vcc_lo, vcc_lo, -2
	s_bcnt1_i32_b32 s12, vcc_lo
	s_lshl_b32 s3, s12, 2
	s_add_i32 s3, s3, 0
	s_add_i32 s3, s3, 0x20100
	v_mov_b32_e32 v4, s3
	ds_read2st64_b32 v[2:3], v4 offset1:1
	ds_read_b32 v5, v4 offset:512
	s_waitcnt lgkmcnt(0)
	v_readfirstlane_b32 s3, v2
	s_sub_i32 s3, s21, s3
	s_abs_i32 s35, s3
	v_readfirstlane_b32 s23, v3
	v_readfirstlane_b32 s44, v5
	s_add_i32 s21, s44, 0xff
	s_ashr_i32 s21, s21, 8
	s_abs_i32 s38, s21
	v_cvt_f32_u32_e32 v2, s38
	s_sub_i32 s39, 0, s38
	s_xor_b32 s34, s3, s21
	s_ashr_i32 s34, s34, 31
	v_rcp_iflag_f32_e32 v2, v2
	s_nop 0
	v_mul_f32_e32 v2, 0x4f7ffffe, v2
	v_cvt_u32_f32_e32 v2, v2
	s_nop 0
	v_readfirstlane_b32 s40, v2
	s_mul_i32 s39, s39, s40
	s_mul_hi_u32 s39, s40, s39
	s_add_i32 s40, s40, s39
	s_mul_hi_u32 s39, s35, s40
	s_mul_i32 s40, s39, s38
	s_sub_i32 s35, s35, s40
	s_add_i32 s40, s39, 1
	s_sub_i32 s41, s35, s38
	s_cmp_ge_u32 s35, s38
	s_cselect_b32 s39, s40, s39
	s_cselect_b32 s35, s41, s35
	s_add_i32 s40, s39, 1
	s_cmp_ge_u32 s35, s38
	s_cselect_b32 s35, s40, s39
	s_xor_b32 s35, s35, s34
	s_sub_i32 s42, s35, s34
	s_mul_i32 s21, s21, s42
	s_sub_i32 s3, s3, s21
	s_lshl_b32 s21, s3, 8
	s_add_i32 s34, s21, s23
	s_ashr_i32 s35, s34, 31
	s_lshl_b64 s[38:39], s[34:35], 11
	v_readlane_b32 s3, v254, 38
	s_add_u32 s38, s3, s38
	v_readlane_b32 s3, v254, 40
	s_addc_u32 s39, s3, s39
	s_lshl_b64 s[40:41], s[12:13], 22
	s_add_u32 s3, s52, s40
	s_addc_u32 s23, s53, s41
	s_ashr_i32 s43, s42, 31
	s_lshl_b64 s[40:41], s[42:43], 19
	s_add_u32 s40, s3, s40
	s_addc_u32 s41, s23, s41
	s_sub_i32 s21, s44, s21
	s_lshl_b32 s3, s42, 8
	s_min_i32 s35, s21, 0x100
